# speedup vs baseline: 1.0407x; 1.0180x over previous
_Z8k3_chainPKfPK15HIP_vector_typeIiLj4EEPKtS6_S0_S0_Pf:
	s_load_dwordx8 s[8:15], s[0:1], 0x0
	s_load_dwordx4 s[4:7], s[0:1], 0x20
	s_load_dwordx2 s[16:17], s[0:1], 0x30
	s_mul_hi_u32 s0, s2, 0xaaaaaaab
	s_lshr_b32 s20, s0, 5
	s_mul_i32 s0, s20, 48
	s_mov_b32 s21, 0
	s_sub_i32 s18, s2, s0
	s_lshl_b64 s[0:1], s[20:21], 13
	s_waitcnt lgkmcnt(0)
	s_add_u32 s2, s10, s0
	v_and_b32_e32 v1, 3, v0
	s_addc_u32 s3, s11, s1
	s_mul_hi_u32 s1, s20, 0x18000
	s_mul_i32 s0, s20, 0x18000
	v_lshlrev_b32_e32 v104, 4, v0
	v_mov_b32_e32 v105, 0
	v_lshl_or_b32 v98, s18, 2, v1
	s_lshl_b64 s[18:19], s[0:1], 4
	v_lshl_add_u64 v[2:3], s[2:3], 0, v[104:105]
	s_add_u32 s0, s8, s18
	s_movk_i32 s8, 0x1000
	v_add_co_u32_e32 v10, vcc, s8, v2
	s_addc_u32 s1, s9, s19
	s_nop 0
	v_addc_co_u32_e32 v11, vcc, 0, v3, vcc
	global_load_dwordx4 v[2:5], v104, s[2:3]
	global_load_dwordx4 v[6:9], v[10:11], off
	s_mul_i32 s2, s20, 0x6000
	s_mul_hi_u32 s3, s20, 0x6000
	s_add_u32 s2, s12, s2
	s_addc_u32 s3, s13, s3
	v_lshl_add_u64 v[10:11], s[2:3], 0, v[104:105]
	s_movk_i32 s8, 0x2000
	v_add_co_u32_e32 v12, vcc, s8, v10
	s_movk_i32 s8, 0x3000
	s_nop 0
	v_addc_co_u32_e32 v13, vcc, 0, v11, vcc
	global_load_dwordx4 v[38:41], v104, s[2:3]
	global_load_dwordx4 v[42:45], v[12:13], off offset:-4096
	global_load_dwordx4 v[46:49], v[12:13], off
	v_add_co_u32_e32 v12, vcc, s8, v10
	v_lshrrev_b32_e32 v110, 2, v0
	s_nop 0
	v_addc_co_u32_e32 v13, vcc, 0, v11, vcc
	v_or_b32_e32 v14, 0x4000, v104
	global_load_dwordx4 v[50:53], v[12:13], off
	global_load_dwordx4 v[54:57], v14, s[2:3]
	s_movk_i32 s2, 0x5000
	v_add_co_u32_e32 v10, vcc, s2, v10
	s_movk_i32 s2, 0xc0
	v_or_b32_e32 v18, 64, v110
	v_addc_co_u32_e32 v11, vcc, 0, v11, vcc
	v_mov_b32_e32 v99, v105
	v_mad_u32_u24 v106, v110, s2, v98
	v_mov_b32_e32 v107, v105
	v_mul_u32_u24_e32 v102, 0xc00, v18
	v_mov_b32_e32 v103, v105
	global_load_dwordx4 v[66:69], v[10:11], off
	v_lshlrev_b64 v[10:11], 4, v[106:107]
	v_lshl_add_u64 v[14:15], s[0:1], 0, v[102:103]
	v_lshlrev_b64 v[16:17], 4, v[98:99]
	v_lshl_add_u64 v[12:13], s[0:1], 0, v[10:11]
	v_lshl_add_u64 v[14:15], v[14:15], 0, v[16:17]
	s_mov_b32 s3, 0x30000
	global_load_dwordx4 v[58:61], v[12:13], off
	global_load_dwordx4 v[62:65], v[14:15], off
	v_add_co_u32_e32 v12, vcc, s3, v14
	s_mov_b32 s3, 0x60000
	s_nop 0
	v_addc_co_u32_e32 v13, vcc, 0, v15, vcc
	v_add_co_u32_e32 v14, vcc, s3, v14
	s_movk_i32 s2, 0xc00
	s_nop 0
	v_addc_co_u32_e32 v15, vcc, 0, v15, vcc
	global_load_dwordx4 v[70:73], v[12:13], off
	global_load_dwordx4 v[74:77], v[14:15], off
	v_mov_b32_e32 v12, 0x90000
	v_mad_u32_u24 v12, v18, s2, v12
	v_mov_b32_e32 v13, v105
	v_mov_b32_e32 v14, 0xc0000
	v_lshl_add_u64 v[12:13], s[0:1], 0, v[12:13]
	v_mad_u32_u24 v100, v18, s2, v14
	v_mov_b32_e32 v101, v105
	v_lshl_add_u64 v[12:13], v[12:13], 0, v[16:17]
	v_lshl_add_u64 v[14:15], s[0:1], 0, v[100:101]
	v_lshl_add_u64 v[14:15], v[14:15], 0, v[16:17]
	global_load_dwordx4 v[78:81], v[12:13], off
	global_load_dwordx4 v[82:85], v[14:15], off
	v_mov_b32_e32 v12, 0xf0000
	v_mad_u32_u24 v96, v18, s2, v12
	v_mov_b32_e32 v97, v105
	v_mov_b32_e32 v14, 0x120000
	v_lshl_add_u64 v[12:13], s[0:1], 0, v[96:97]
	v_mad_u32_u24 v94, v18, s2, v14
	v_mov_b32_e32 v95, v105
	v_lshl_add_u64 v[12:13], v[12:13], 0, v[16:17]
	v_lshl_add_u64 v[14:15], s[0:1], 0, v[94:95]
	v_lshl_add_u64 v[14:15], v[14:15], 0, v[16:17]
	global_load_dwordx4 v[86:89], v[12:13], off
	global_load_dwordx4 v[90:93], v[14:15], off
	s_waitcnt vmcnt(15)
	ds_write_b128 v104, v[2:5] offset:57408
	s_waitcnt vmcnt(14)
	ds_write_b128 v104, v[6:9] offset:61504
	v_lshl_add_u64 v[2:3], s[6:7], 0, v[10:11]
	s_waitcnt lgkmcnt(0)
	s_barrier
	global_load_dwordx4 v[34:37], v[2:3], off
	v_lshl_add_u64 v[2:3], s[4:5], 0, v[10:11]
	v_add_u32_e32 v4, 0x3000, v106
	v_mov_b32_e32 v5, v105
	v_lshl_add_u64 v[4:5], v[4:5], 4, s[4:5]
	global_load_dwordx4 v[30:33], v[2:3], off
	global_load_dwordx4 v[26:29], v[4:5], off
	v_add_u32_e32 v2, 0x6000, v106
	v_mov_b32_e32 v3, v105
	v_lshl_add_u64 v[2:3], v[2:3], 4, s[4:5]
	v_add_u32_e32 v4, 0x9000, v106
	v_mov_b32_e32 v5, v105
	v_lshl_add_u64 v[4:5], v[4:5], 4, s[4:5]
	global_load_dwordx4 v[22:25], v[2:3], off
	global_load_dwordx4 v[18:21], v[4:5], off
	v_add_u32_e32 v2, 0xc000, v106
	v_mov_b32_e32 v3, v105
	v_lshl_add_u64 v[2:3], v[2:3], 4, s[4:5]
	v_add_u32_e32 v4, 0xf000, v106
	v_mov_b32_e32 v5, v105
	v_lshl_add_u64 v[4:5], v[4:5], 4, s[4:5]
	global_load_dwordx4 v[14:17], v[2:3], off
	global_load_dwordx4 v[10:13], v[4:5], off
	v_add_u32_e32 v2, 0x12000, v106
	v_mov_b32_e32 v3, v105
	v_lshl_add_u64 v[108:109], v[2:3], 4, s[4:5]
	v_add_u32_e32 v2, 0x15000, v106
	v_lshl_add_u64 v[106:107], v[2:3], 4, s[4:5]
	global_load_dwordx4 v[6:9], v[108:109], off
	global_load_dwordx4 v[2:5], v[106:107], off
	v_bfe_u32 v113, v0, 5, 1
	v_lshrrev_b32_e32 v115, 6, v0
	v_lshlrev_b32_e32 v112, 2, v113
	v_and_b32_e32 v111, 31, v0
	v_or_b32_e32 v116, v112, v115
	v_lshl_or_b32 v120, v116, 5, v111
	v_lshlrev_b32_e32 v108, 4, v120
	ds_read_b32 v140, v108 offset:57420
	ds_read_b32 v141, v108 offset:61516
	ds_read_u16 v158, v108 offset:57408
	ds_read_u16 v159, v108 offset:61504
	v_lshlrev_b32_e32 v142, 9, v116
	v_add_u32_e32 v142, 0x200, v142
	v_add_u32_e32 v143, 0x1000, v142
	v_mov_b32_e32 v152, 0x2000
	s_waitcnt lgkmcnt(0)
	v_cmp_lt_u32_e64 s[28:29], 12, v158
	v_cmp_lt_u32_e64 s[30:31], 12, v159
	v_ffbl_b32_e32 v153, v140
	v_ffbl_b32_e32 v154, v141
	v_cmp_ne_u32_e32 vcc, 0, v140
	v_cmp_ne_u32_e64 s[22:23], 0, v141
	v_lshl_add_u32 v153, v153, 4, v142
	v_lshl_add_u32 v154, v154, 4, v143
	v_cndmask_b32_e32 v144, v152, v153, vcc
	v_cndmask_b32_e64 v160, v152, v154, s[22:23]
	v_add_u32_e32 v153, -1, v140
	v_add_u32_e32 v154, -1, v141
	v_and_b32_e32 v140, v153, v140
	v_and_b32_e32 v141, v154, v141
	v_ffbl_b32_e32 v153, v140
	v_ffbl_b32_e32 v154, v141
	v_cmp_ne_u32_e32 vcc, 0, v140
	v_cmp_ne_u32_e64 s[22:23], 0, v141
	v_lshl_add_u32 v153, v153, 4, v142
	v_lshl_add_u32 v154, v154, 4, v143
	v_cndmask_b32_e32 v145, v152, v153, vcc
	v_cndmask_b32_e64 v161, v152, v154, s[22:23]
	v_add_u32_e32 v153, -1, v140
	v_add_u32_e32 v154, -1, v141
	v_and_b32_e32 v140, v153, v140
	v_and_b32_e32 v141, v154, v141
	v_ffbl_b32_e32 v153, v140
	v_ffbl_b32_e32 v154, v141
	v_cmp_ne_u32_e32 vcc, 0, v140
	v_cmp_ne_u32_e64 s[22:23], 0, v141
	v_lshl_add_u32 v153, v153, 4, v142
	v_lshl_add_u32 v154, v154, 4, v143
	v_cndmask_b32_e32 v146, v152, v153, vcc
	v_cndmask_b32_e64 v162, v152, v154, s[22:23]
	v_add_u32_e32 v153, -1, v140
	v_add_u32_e32 v154, -1, v141
	v_and_b32_e32 v140, v153, v140
	v_and_b32_e32 v141, v154, v141
	v_ffbl_b32_e32 v153, v140
	v_ffbl_b32_e32 v154, v141
	v_cmp_ne_u32_e32 vcc, 0, v140
	v_cmp_ne_u32_e64 s[22:23], 0, v141
	v_lshl_add_u32 v153, v153, 4, v142
	v_lshl_add_u32 v154, v154, 4, v143
	v_cndmask_b32_e32 v147, v152, v153, vcc
	v_cndmask_b32_e64 v163, v152, v154, s[22:23]
	v_add_u32_e32 v153, -1, v140
	v_add_u32_e32 v154, -1, v141
	v_and_b32_e32 v140, v153, v140
	v_and_b32_e32 v141, v154, v141
	v_ffbl_b32_e32 v153, v140
	v_ffbl_b32_e32 v154, v141
	v_cmp_ne_u32_e32 vcc, 0, v140
	v_cmp_ne_u32_e64 s[22:23], 0, v141
	v_lshl_add_u32 v153, v153, 4, v142
	v_lshl_add_u32 v154, v154, 4, v143
	v_cndmask_b32_e32 v148, v152, v153, vcc
	v_cndmask_b32_e64 v164, v152, v154, s[22:23]
	v_add_u32_e32 v153, -1, v140
	v_add_u32_e32 v154, -1, v141
	v_and_b32_e32 v140, v153, v140
	v_and_b32_e32 v141, v154, v141
	v_lshl_or_b32 v144, v145, 16, v144
	v_lshl_or_b32 v145, v147, 16, v146
	v_lshl_or_b32 v146, v152, 16, v148
	v_mov_b32_e32 v147, v140
	v_lshl_or_b32 v160, v161, 16, v160
	v_lshl_or_b32 v161, v163, 16, v162
	v_lshl_or_b32 v162, v152, 16, v164
	v_mov_b32_e32 v163, v141
	v_add_u32_e32 v153, 0x118c0, v108
	ds_write_b128 v153, v[144:147]
	ds_write_b128 v153, v[160:163] offset:4096
	ds_read_b64 v[106:107], v108 offset:57408
	ds_read_u16 v118, v108 offset:57410
	v_and_b32_e32 v114, 63, v0
	v_and_b32_e32 v0, 32, v0
	v_add_u32_e32 v117, 0xe040, v108
	v_mov_b32_e32 v108, -1
	v_mov_b32_e32 v119, v105
	s_branch .LBB2_2

.LBB2_12:
	s_or_b64 exec, exec, s[12:13]
	v_lshlrev_b32_e32 v106, 9, v119
	v_ffbl_b32_e32 v107, v107
	v_ffbl_b32_e32 v108, v108
	v_lshlrev_b32_e32 v116, 25, v119
	v_lshl_or_b32 v107, v107, 4, v106
	v_mov_b32_e32 v109, 0x2000
	v_lshl_or_b32 v108, v108, 20, v116
	v_bfrev_b32_e32 v116, 4
	v_ffbl_b32_e32 v0, v0
	v_cndmask_b32_e64 v107, v107, v109, s[8:9]
	v_cndmask_b32_e64 v108, v108, v116, s[4:5]
	v_lshl_or_b32 v0, v0, 4, v106
	v_cndmask_b32_e32 v0, v0, v109, vcc
	v_or_b32_e32 v106, v108, v107
	v_mov_b32_e32 v108, 0x800000
	v_lshlrev_b32_e32 v107, 16, v117
	v_cndmask_b32_e64 v108, 0, v108, s[6:7]
	s_waitcnt lgkmcnt(2)
	v_lshl_or_b32 v0, v118, 24, v0
	v_or3_b32 v0, v0, v108, v107
	ds_write2_b32 v105, v106, v0 offset0:1 offset1:3
	v_cmp_ne_u32_e32 vcc, 0, v140
	v_cmp_ne_u32_e64 s[22:23], 0, v141
	v_lshlrev_b32_e32 v150, 5, v113
	v_lshl_add_u32 v155, v113, 2, v115
	v_lshlrev_b32_e32 v155, 2, v155
	v_add_u32_e32 v155, 0x11840, v155
	v_lshrrev_b64 v[146:147], v150, vcc
	v_lshrrev_b64 v[156:157], v150, s[22:23]
	v_mov_b32_e32 v151, 0x400
	v_cmp_ne_u32_e32 vcc, 0, v146
	v_cmp_ne_u32_e64 s[22:23], 0, v156
	s_nop 1
	v_cndmask_b32_e32 v146, 0, v151, vcc
	v_cndmask_b32_e64 v156, 0, v151, s[22:23]
	v_lshrrev_b64 v[148:149], v150, s[28:29]
	v_lshrrev_b64 v[152:153], v150, s[30:31]
	v_mov_b32_e32 v154, 0x800
	v_cmp_ne_u32_e32 vcc, 0, v148
	v_cmp_ne_u32_e64 s[22:23], 0, v152
	s_nop 1
	v_cndmask_b32_e32 v148, 0, v154, vcc
	v_cndmask_b32_e64 v152, 0, v154, s[22:23]
	v_or_b32_e32 v146, v146, v148
	v_or_b32_e32 v156, v156, v152
	v_cmp_eq_u32_e32 vcc, 0, v111
	s_and_saveexec_b64 s[22:23], vcc
	ds_or_b32 v155, v146
	ds_or_b32 v155, v156 offset:32
	s_or_b64 exec, exec, s[22:23]
	s_movk_i32 s2, 0x2010
	v_mul_u32_u24_e32 v105, 0x2010, v115
	v_cmp_eq_u32_e32 vcc, 0, v114
	s_waitcnt vmcnt(22)
	ds_write_b128 v104, v[38:41] offset:32832
	s_waitcnt vmcnt(21)
	ds_write_b128 v104, v[42:45] offset:36928
	s_waitcnt vmcnt(20)
	ds_write_b128 v104, v[46:49] offset:41024
	s_waitcnt vmcnt(19)
	ds_write_b128 v104, v[50:53] offset:45120
	s_waitcnt vmcnt(18)
	ds_write_b128 v104, v[54:57] offset:49216
	s_waitcnt vmcnt(17)
	ds_write_b128 v104, v[66:69] offset:53312
	s_and_saveexec_b64 s[0:1], vcc
	v_mov_b32_e32 v38, 0
	v_mov_b32_e32 v39, v38
	v_mov_b32_e32 v40, v38
	v_mov_b32_e32 v41, v38
	ds_write_b128 v105, v[38:41] offset:8192
	s_or_b64 exec, exec, s[0:1]
	v_lshlrev_b32_e32 v40, 3, v113
	v_lshlrev_b32_e32 v67, 4, v110
	v_or_b32_e32 v38, 0x1e0, v111
	v_or_b32_e32 v0, 0x8040, v40
	v_mad_u32_u24 v66, v1, s2, v67
	v_mad_u32_u24 v38, v38, 48, v0
	s_waitcnt vmcnt(16)
	ds_write_b128 v66, v[58:61]
	s_waitcnt vmcnt(15)
	ds_write_b128 v66, v[62:65] offset:1024
	s_waitcnt vmcnt(14)
	ds_write_b128 v66, v[70:73] offset:2048
	s_waitcnt vmcnt(13)
	ds_write_b128 v66, v[74:77] offset:3072
	s_waitcnt vmcnt(12)
	ds_write_b128 v66, v[78:81] offset:4096
	s_waitcnt vmcnt(11)
	ds_write_b128 v66, v[82:85] offset:5120
	s_waitcnt vmcnt(10)
	ds_write_b128 v66, v[86:89] offset:6144
	s_waitcnt vmcnt(9)
	ds_write_b128 v66, v[90:93] offset:7168
	v_lshl_add_u32 v116, v113, 3, v105
	v_or_b32_e32 v106, 0x1e0, v111
	v_lshlrev_b32_e32 v138, 4, v106
	v_add_u32_e32 v139, 0x118c0, v138
	v_mul_u32_u24_e32 v156, 48, v106
	v_add_u32_e32 v156, v0, v156
	v_mov_b32_e32 v157, 0x1187c
	v_add_u32_e32 v137, v116, v138
	v_add_u32_e32 v138, 0x200, v138
	v_lshlrev_b32_e32 v160, 4, v111
	v_lshlrev_b32_e32 v161, 3, v111
	v_add_u32_e32 v161, 0x118c0, v161
	v_mul_u32_u24_e32 v162, 48, v111
	v_add_u32_e32 v162, v0, v162
	v_mov_b32_e32 v163, 0x11840
	v_mul_hi_u32_u24_e32 v159, 0x410, v111
	v_mul_u32_u24_e32 v158, 0x410, v111
	v_mov_b32_e32 v107, 0x82000
	v_mad_u64_u32 v[158:159], s[0:1], s20, v107, v[158:159]
	v_lshlrev_b32_e32 v107, 3, v113
	v_or_b32_e32 v158, v158, v107
	v_lshl_add_u64 v[158:159], s[14:15], 0, v[158:159]
	s_mov_b64 s[0:1], 0x79e30
	s_mov_b32 s2, 0xffff7e00
	s_mov_b32 s3, -1
	v_lshl_add_u64 v[158:159], v[158:159], 0, s[0:1]
	v_lshl_add_u32 v107, v114, 2, v163
	v_add_u32_e32 v107, -8, v107
	s_waitcnt lgkmcnt(0)
	s_barrier
	ds_read_b128 v[38:41], v138 offset:56896
	ds_read_b128 v[42:45], v139
	ds_read2_b64 v[56:59], v156 offset1:2
	ds_read_b32 v60, v107
	v_add_u32_e32 v156, 0xfffffa00, v156
	ds_read2_b64 v[52:55], v156 offset1:2
	v_add_u32_e32 v106, -2, v114
	v_cmp_gt_u32_e32 vcc, 16, v106
	s_waitcnt lgkmcnt(0)
	v_cndmask_b32_e32 v60, 0, v60, vcc
	s_nop 1
	v_readlane_b32 s4, v60, 17
	v_readlane_b32 s21, v60, 16
	v_add_u32_sdwa v92, v105, v56 dst_sel:DWORD dst_unused:UNUSED_PAD src0_sel:DWORD src1_sel:WORD_0
	v_add_u32_sdwa v93, v105, v56 dst_sel:DWORD dst_unused:UNUSED_PAD src0_sel:DWORD src1_sel:WORD_1
	v_add_u32_sdwa v106, v105, v57 dst_sel:DWORD dst_unused:UNUSED_PAD src0_sel:DWORD src1_sel:WORD_0
	v_add_u32_sdwa v107, v105, v57 dst_sel:DWORD dst_unused:UNUSED_PAD src0_sel:DWORD src1_sel:WORD_1
	v_add_u32_sdwa v108, v105, v58 dst_sel:DWORD dst_unused:UNUSED_PAD src0_sel:DWORD src1_sel:WORD_0
	v_add_u32_sdwa v109, v105, v58 dst_sel:DWORD dst_unused:UNUSED_PAD src0_sel:DWORD src1_sel:WORD_1
	ds_read_b128 v[120:123], v92
	ds_read_b128 v[124:127], v93
	ds_read_b128 v[128:131], v106
	ds_read_b128 v[132:135], v107
	ds_read_b128 v[140:143], v108
	ds_read_b128 v[144:147], v109
	v_add_u32_sdwa v88, v116, v42 dst_sel:DWORD dst_unused:UNUSED_PAD src0_sel:DWORD src1_sel:WORD_0
	v_add_u32_sdwa v89, v116, v42 dst_sel:DWORD dst_unused:UNUSED_PAD src0_sel:DWORD src1_sel:WORD_1
	v_add_u32_sdwa v90, v116, v43 dst_sel:DWORD dst_unused:UNUSED_PAD src0_sel:DWORD src1_sel:WORD_0
	v_add_u32_sdwa v91, v116, v43 dst_sel:DWORD dst_unused:UNUSED_PAD src0_sel:DWORD src1_sel:WORD_1
	v_add_u32_sdwa v173, v116, v44 dst_sel:DWORD dst_unused:UNUSED_PAD src0_sel:DWORD src1_sel:WORD_0
	v_bfe_u32 v117, v41, 16, 7
	v_add_u32_sdwa v118, v116, v39 dst_sel:DWORD dst_unused:UNUSED_PAD src0_sel:DWORD src1_sel:WORD_0
	v_add_u32_sdwa v119, v116, v39 dst_sel:DWORD dst_unused:UNUSED_PAD src0_sel:DWORD src1_sel:WORD_1
	v_add_u32_sdwa v136, v116, v41 dst_sel:DWORD dst_unused:UNUSED_PAD src0_sel:DWORD src1_sel:WORD_0
	s_and_b32 s9, s4, 0xff
	s_waitcnt lgkmcnt(0)
	v_pk_add_f32 v[120:121], v[120:121], v[124:125]
	v_pk_add_f32 v[122:123], v[122:123], v[126:127]
	v_pk_add_f32 v[128:129], v[128:129], v[132:133]
	v_pk_add_f32 v[130:131], v[130:131], v[134:135]
	v_pk_add_f32 v[140:141], v[140:141], v[144:145]
	v_pk_add_f32 v[142:143], v[142:143], v[146:147]
	s_and_b32 s24, s4, 0x900
	s_cbranch_scc1 .Lfarx_pre
.Lfarslow_ret_pre:
	v_pk_add_f32 v[120:121], v[120:121], v[128:129]
	v_pk_add_f32 v[122:123], v[122:123], v[130:131]
	v_pk_add_f32 v[120:121], v[120:121], v[140:141]
	v_pk_add_f32 v[122:123], v[122:123], v[142:143]
	s_nop 1
	v_permlane32_swap_b32_e32 v120, v122
	v_permlane32_swap_b32_e32 v121, v123
	v_pk_add_f32 v[176:177], v[120:121], v[122:123]
	v_add_u32_e32 v138, 0xfffffe00, v138
	v_add_u32_e32 v139, 0xfffffe00, v139
	v_add_u32_e32 v156, 0xfffffa00, v156
	v_lshl_add_u64 v[158:159], v[158:159], 0, s[2:3]
	s_mov_b32 s5, 15
	s_mov_b32 s5, 15
.Lit_A:
	ds_read_b64 v[68:69], v88
	ds_read_b64 v[70:71], v89
	ds_read_b64 v[72:73], v90
	ds_read_b64 v[74:75], v91
	ds_read_b64 v[174:175], v173
	v_add_u32_sdwa v92, v105, v52 dst_sel:DWORD dst_unused:UNUSED_PAD src0_sel:DWORD src1_sel:WORD_0
	v_add_u32_sdwa v93, v105, v52 dst_sel:DWORD dst_unused:UNUSED_PAD src0_sel:DWORD src1_sel:WORD_1
	v_add_u32_sdwa v106, v105, v53 dst_sel:DWORD dst_unused:UNUSED_PAD src0_sel:DWORD src1_sel:WORD_0
	v_add_u32_sdwa v107, v105, v53 dst_sel:DWORD dst_unused:UNUSED_PAD src0_sel:DWORD src1_sel:WORD_1
	v_add_u32_sdwa v108, v105, v54 dst_sel:DWORD dst_unused:UNUSED_PAD src0_sel:DWORD src1_sel:WORD_0
	v_add_u32_sdwa v109, v105, v54 dst_sel:DWORD dst_unused:UNUSED_PAD src0_sel:DWORD src1_sel:WORD_1
	ds_read_b128 v[120:123], v92
	ds_read_b128 v[124:127], v93
	ds_read_b128 v[128:131], v106
	ds_read_b128 v[132:135], v107
	ds_read_b128 v[140:143], v108
	ds_read_b128 v[144:147], v109
	s_waitcnt lgkmcnt(6)
	v_pk_add_f32 v[76:77], v[176:177], v[68:69]
	v_pk_add_f32 v[78:79], v[70:71], v[72:73]
	v_pk_add_f32 v[74:75], v[74:75], v[174:175]
	v_pk_add_f32 v[76:77], v[76:77], v[78:79]
	ds_read_b128 v[46:49], v138 offset:56896
	v_pk_add_f32 v[76:77], v[76:77], v[74:75]
	ds_read_b128 v[180:183], v139
	s_bitcmp1_b32 s4, 10
	s_cbranch_scc1 .Lnearslow_A

.Lfarslow_ret_A:
	v_pk_add_f32 v[120:121], v[120:121], v[128:129]
	v_pk_add_f32 v[122:123], v[122:123], v[130:131]
	v_pk_add_f32 v[120:121], v[120:121], v[140:141]
	v_pk_add_f32 v[122:123], v[122:123], v[142:143]
	v_add_u32_e32 v138, 0xfffffe00, v138
	v_add_u32_e32 v139, 0xfffffe00, v139
	v_permlane32_swap_b32_e32 v120, v122
	v_permlane32_swap_b32_e32 v121, v123
	v_pk_add_f32 v[62:63], v[120:121], v[122:123]
	s_bitcmp1_b32 s4, 9
	s_cbranch_scc1 .Lslowlev_A
	s_waitcnt lgkmcnt(0)
	v_pk_fma_f32 v[80:81], v[40:41], v[82:83], v[78:79] op_sel_hi:[0,1,1]
	s_cmp_lt_u32 s9, 2
	v_pk_fma_f32 v[80:81], v[40:41], v[84:85], v[80:81] op_sel_hi:[0,1,1]
	s_mov_b64 exec, s[6:7]
	v_pk_fma_f32 v[80:81], v[40:41], v[86:87], v[80:81] op_sel_hi:[0,1,1]
	ds_write_b64 v137, v[80:81]
	s_mov_b64 exec, -1
	s_cbranch_scc1 .Lnp_A
	ds_read_b64 v[82:83], v118
	ds_read_b64 v[84:85], v119
	ds_read_b64 v[86:87], v136
	v_add_u32_sdwa v88, v116, v180 dst_sel:DWORD dst_unused:UNUSED_PAD src0_sel:DWORD src1_sel:WORD_0
	v_add_u32_sdwa v89, v116, v180 dst_sel:DWORD dst_unused:UNUSED_PAD src0_sel:DWORD src1_sel:WORD_1
	v_add_u32_sdwa v90, v116, v181 dst_sel:DWORD dst_unused:UNUSED_PAD src0_sel:DWORD src1_sel:WORD_0
	v_add_u32_sdwa v91, v116, v181 dst_sel:DWORD dst_unused:UNUSED_PAD src0_sel:DWORD src1_sel:WORD_1
	v_add_u32_sdwa v173, v116, v182 dst_sel:DWORD dst_unused:UNUSED_PAD src0_sel:DWORD src1_sel:WORD_0
	v_bfe_u32 v168, v49, 16, 7
	v_add_u32_sdwa v169, v116, v47 dst_sel:DWORD dst_unused:UNUSED_PAD src0_sel:DWORD src1_sel:WORD_0
	v_add_u32_sdwa v170, v116, v47 dst_sel:DWORD dst_unused:UNUSED_PAD src0_sel:DWORD src1_sel:WORD_1
	v_add_u32_sdwa v171, v116, v49 dst_sel:DWORD dst_unused:UNUSED_PAD src0_sel:DWORD src1_sel:WORD_0
	v_add_u32_e32 v156, 0xfffffa00, v156
	v_add_u32_e32 v172, 0xfffffe00, v137
	v_readlane_b32 s4, v60, s5
	v_max_i32_e32 v156, v156, v162
	v_lshl_add_u64 v[158:159], v[158:159], 0, s[2:3]
	s_and_b32 s23, s21, 0xff
	s_waitcnt lgkmcnt(0)
	v_pk_fma_f32 v[80:81], v[40:41], v[82:83], v[78:79] op_sel_hi:[0,1,1]
	s_cmp_lt_u32 s9, 3
	v_pk_fma_f32 v[80:81], v[40:41], v[84:85], v[80:81] op_sel_hi:[0,1,1]
	s_mov_b64 exec, s[26:27]
	v_pk_fma_f32 v[80:81], v[40:41], v[86:87], v[80:81] op_sel_hi:[0,1,1]
	ds_write_b64 v137, v[80:81]
	s_mov_b64 exec, -1
	s_cbranch_scc1 .Lbot_A
	s_mov_b32 s8, 3

.Lit_B:
	ds_read_b64 v[68:69], v88
	ds_read_b64 v[70:71], v89
	ds_read_b64 v[72:73], v90
	ds_read_b64 v[74:75], v91
	ds_read_b64 v[174:175], v173
	v_add_u32_sdwa v92, v105, v56 dst_sel:DWORD dst_unused:UNUSED_PAD src0_sel:DWORD src1_sel:WORD_0
	v_add_u32_sdwa v93, v105, v56 dst_sel:DWORD dst_unused:UNUSED_PAD src0_sel:DWORD src1_sel:WORD_1
	v_add_u32_sdwa v106, v105, v57 dst_sel:DWORD dst_unused:UNUSED_PAD src0_sel:DWORD src1_sel:WORD_0
	v_add_u32_sdwa v107, v105, v57 dst_sel:DWORD dst_unused:UNUSED_PAD src0_sel:DWORD src1_sel:WORD_1
	v_add_u32_sdwa v108, v105, v58 dst_sel:DWORD dst_unused:UNUSED_PAD src0_sel:DWORD src1_sel:WORD_0
	v_add_u32_sdwa v109, v105, v58 dst_sel:DWORD dst_unused:UNUSED_PAD src0_sel:DWORD src1_sel:WORD_1
	ds_read_b128 v[120:123], v92
	ds_read_b128 v[124:127], v93
	ds_read_b128 v[128:131], v106
	ds_read_b128 v[132:135], v107
	ds_read_b128 v[140:143], v108
	ds_read_b128 v[144:147], v109
	s_waitcnt lgkmcnt(6)
	v_pk_add_f32 v[76:77], v[62:63], v[68:69]
	v_pk_add_f32 v[78:79], v[70:71], v[72:73]
	v_pk_add_f32 v[74:75], v[74:75], v[174:175]
	v_pk_add_f32 v[76:77], v[76:77], v[78:79]
	ds_read_b128 v[38:41], v138 offset:56896
	v_pk_add_f32 v[76:77], v[76:77], v[74:75]
	ds_read_b128 v[42:45], v139
	s_bitcmp1_b32 s21, 10
	s_cbranch_scc1 .Lnearslow_B

.Lfarslow_ret_B:
	v_pk_add_f32 v[120:121], v[120:121], v[128:129]
	v_pk_add_f32 v[122:123], v[122:123], v[130:131]
	v_pk_add_f32 v[120:121], v[120:121], v[140:141]
	v_pk_add_f32 v[122:123], v[122:123], v[142:143]
	v_add_u32_e32 v138, 0xfffffe00, v138
	v_add_u32_e32 v139, 0xfffffe00, v139
	v_permlane32_swap_b32_e32 v120, v122
	v_permlane32_swap_b32_e32 v121, v123
	v_pk_add_f32 v[176:177], v[120:121], v[122:123]
	s_bitcmp1_b32 s21, 9
	s_cbranch_scc1 .Lslowlev_B
	s_waitcnt lgkmcnt(0)
	v_pk_fma_f32 v[80:81], v[48:49], v[82:83], v[78:79] op_sel_hi:[0,1,1]
	s_cmp_lt_u32 s23, 2
	v_pk_fma_f32 v[80:81], v[48:49], v[84:85], v[80:81] op_sel_hi:[0,1,1]
	s_mov_b64 exec, s[6:7]
	v_pk_fma_f32 v[80:81], v[48:49], v[86:87], v[80:81] op_sel_hi:[0,1,1]
	ds_write_b64 v172, v[80:81]
	s_mov_b64 exec, -1
	s_cbranch_scc1 .Lnp_B
	ds_read_b64 v[82:83], v169
	ds_read_b64 v[84:85], v170
	ds_read_b64 v[86:87], v171
	v_add_u32_sdwa v88, v116, v42 dst_sel:DWORD dst_unused:UNUSED_PAD src0_sel:DWORD src1_sel:WORD_0
	v_add_u32_sdwa v89, v116, v42 dst_sel:DWORD dst_unused:UNUSED_PAD src0_sel:DWORD src1_sel:WORD_1
	v_add_u32_sdwa v90, v116, v43 dst_sel:DWORD dst_unused:UNUSED_PAD src0_sel:DWORD src1_sel:WORD_0
	v_add_u32_sdwa v91, v116, v43 dst_sel:DWORD dst_unused:UNUSED_PAD src0_sel:DWORD src1_sel:WORD_1
	v_add_u32_sdwa v173, v116, v44 dst_sel:DWORD dst_unused:UNUSED_PAD src0_sel:DWORD src1_sel:WORD_0
	v_bfe_u32 v117, v41, 16, 7
	v_add_u32_sdwa v118, v116, v39 dst_sel:DWORD dst_unused:UNUSED_PAD src0_sel:DWORD src1_sel:WORD_0
	v_add_u32_sdwa v119, v116, v39 dst_sel:DWORD dst_unused:UNUSED_PAD src0_sel:DWORD src1_sel:WORD_1
	v_add_u32_sdwa v136, v116, v41 dst_sel:DWORD dst_unused:UNUSED_PAD src0_sel:DWORD src1_sel:WORD_0
	v_add_u32_e32 v156, 0xfffffa00, v156
	v_add_u32_e32 v137, 0xfffffe00, v172
	v_readlane_b32 s21, v60, s5
	v_max_i32_e32 v156, v156, v162
	v_lshl_add_u64 v[158:159], v[158:159], 0, s[2:3]
	s_and_b32 s9, s4, 0xff
	s_waitcnt lgkmcnt(0)
	v_pk_fma_f32 v[80:81], v[48:49], v[82:83], v[78:79] op_sel_hi:[0,1,1]
	s_cmp_lt_u32 s23, 3
	v_pk_fma_f32 v[80:81], v[48:49], v[84:85], v[80:81] op_sel_hi:[0,1,1]
	s_mov_b64 exec, s[26:27]
	v_pk_fma_f32 v[80:81], v[48:49], v[86:87], v[80:81] op_sel_hi:[0,1,1]
	ds_write_b64 v172, v[80:81]
	s_mov_b64 exec, -1
	s_cbranch_scc1 .Lbot_B
	s_mov_b32 s8, 3

.Lnp_A:
	s_waitcnt lgkmcnt(0)
	v_add_u32_sdwa v88, v116, v180 dst_sel:DWORD dst_unused:UNUSED_PAD src0_sel:DWORD src1_sel:WORD_0
	v_add_u32_sdwa v89, v116, v180 dst_sel:DWORD dst_unused:UNUSED_PAD src0_sel:DWORD src1_sel:WORD_1
	v_add_u32_sdwa v90, v116, v181 dst_sel:DWORD dst_unused:UNUSED_PAD src0_sel:DWORD src1_sel:WORD_0
	v_add_u32_sdwa v91, v116, v181 dst_sel:DWORD dst_unused:UNUSED_PAD src0_sel:DWORD src1_sel:WORD_1
	v_add_u32_sdwa v173, v116, v182 dst_sel:DWORD dst_unused:UNUSED_PAD src0_sel:DWORD src1_sel:WORD_0
	v_bfe_u32 v168, v49, 16, 7
	v_add_u32_sdwa v169, v116, v47 dst_sel:DWORD dst_unused:UNUSED_PAD src0_sel:DWORD src1_sel:WORD_0
	v_add_u32_sdwa v170, v116, v47 dst_sel:DWORD dst_unused:UNUSED_PAD src0_sel:DWORD src1_sel:WORD_1
	v_add_u32_sdwa v171, v116, v49 dst_sel:DWORD dst_unused:UNUSED_PAD src0_sel:DWORD src1_sel:WORD_0
	v_add_u32_e32 v156, 0xfffffa00, v156
	v_add_u32_e32 v172, 0xfffffe00, v137
	v_readlane_b32 s4, v60, s5
	v_max_i32_e32 v156, v156, v162
	v_lshl_add_u64 v[158:159], v[158:159], 0, s[2:3]
	s_and_b32 s23, s21, 0xff
	s_branch .Lbot_A
.Lnp_B:
	s_waitcnt lgkmcnt(0)
	v_add_u32_sdwa v88, v116, v42 dst_sel:DWORD dst_unused:UNUSED_PAD src0_sel:DWORD src1_sel:WORD_0
	v_add_u32_sdwa v89, v116, v42 dst_sel:DWORD dst_unused:UNUSED_PAD src0_sel:DWORD src1_sel:WORD_1
	v_add_u32_sdwa v90, v116, v43 dst_sel:DWORD dst_unused:UNUSED_PAD src0_sel:DWORD src1_sel:WORD_0
	v_add_u32_sdwa v91, v116, v43 dst_sel:DWORD dst_unused:UNUSED_PAD src0_sel:DWORD src1_sel:WORD_1
	v_add_u32_sdwa v173, v116, v44 dst_sel:DWORD dst_unused:UNUSED_PAD src0_sel:DWORD src1_sel:WORD_0
	v_bfe_u32 v117, v41, 16, 7
	v_add_u32_sdwa v118, v116, v39 dst_sel:DWORD dst_unused:UNUSED_PAD src0_sel:DWORD src1_sel:WORD_0
	v_add_u32_sdwa v119, v116, v39 dst_sel:DWORD dst_unused:UNUSED_PAD src0_sel:DWORD src1_sel:WORD_1
	v_add_u32_sdwa v136, v116, v41 dst_sel:DWORD dst_unused:UNUSED_PAD src0_sel:DWORD src1_sel:WORD_0
	v_add_u32_e32 v156, 0xfffffa00, v156
	v_add_u32_e32 v137, 0xfffffe00, v172
	v_readlane_b32 s21, v60, s5
	v_max_i32_e32 v156, v156, v162
	v_lshl_add_u64 v[158:159], v[158:159], 0, s[2:3]
	s_and_b32 s9, s4, 0xff
	s_branch .Lbot_B

.Lnearslow_A:
	v_mov_b32_e32 v165, v45
	v_lshlrev_b32_e32 v166, 4, v111
	v_sub_u32_e32 v166, v137, v166
	v_add_u32_e32 v166, 0x200, v166
	v_cmp_ne_u32_e32 vcc, 0, v165
	s_and_saveexec_b64 s[12:13], vcc
	s_cbranch_execz .Lnearslow_end_A

.Lnearslow_B:
	v_mov_b32_e32 v165, v183
	v_lshlrev_b32_e32 v166, 4, v111
	v_sub_u32_e32 v166, v172, v166
	v_add_u32_e32 v166, 0x200, v166
	v_cmp_ne_u32_e32 vcc, 0, v165
	s_and_saveexec_b64 s[12:13], vcc
	s_cbranch_execz .Lnearslow_end_B

	.amdhsa_kernel _Z8k3_chainPKfPK15HIP_vector_typeIiLj4EEPKtS6_S0_S0_Pf
		.amdhsa_group_segment_fixed_size 80064
		.amdhsa_private_segment_fixed_size 0
		.amdhsa_kernarg_size 56
		.amdhsa_user_sgpr_count 2
		.amdhsa_user_sgpr_dispatch_ptr 0
		.amdhsa_user_sgpr_queue_ptr 0
		.amdhsa_user_sgpr_kernarg_segment_ptr 1
		.amdhsa_user_sgpr_dispatch_id 0
		.amdhsa_user_sgpr_kernarg_preload_length 0
		.amdhsa_user_sgpr_kernarg_preload_offset 0
		.amdhsa_user_sgpr_private_segment_size 0
		.amdhsa_uses_dynamic_stack 0
		.amdhsa_enable_private_segment 0
		.amdhsa_system_sgpr_workgroup_id_x 1
		.amdhsa_system_sgpr_workgroup_id_y 0
		.amdhsa_system_sgpr_workgroup_id_z 0
		.amdhsa_system_sgpr_workgroup_info 0
		.amdhsa_system_vgpr_workitem_id 0
		.amdhsa_next_free_vgpr 185
		.amdhsa_next_free_sgpr 96
		.amdhsa_accum_offset 184
		.amdhsa_reserve_vcc 1
		.amdhsa_float_round_mode_32 0
		.amdhsa_float_round_mode_16_64 0
		.amdhsa_float_denorm_mode_32 3
		.amdhsa_float_denorm_mode_16_64 3
		.amdhsa_dx10_clamp 1
		.amdhsa_ieee_mode 1
		.amdhsa_fp16_overflow 0
		.amdhsa_tg_split 0
		.amdhsa_exception_fp_ieee_invalid_op 0
		.amdhsa_exception_fp_denorm_src 0
		.amdhsa_exception_fp_ieee_div_zero 0
		.amdhsa_exception_fp_ieee_overflow 0
		.amdhsa_exception_fp_ieee_underflow 0
		.amdhsa_exception_fp_ieee_inexact 0
		.amdhsa_exception_int_div_zero 0
	.end_amdhsa_kernel

amdhsa.kernels:
  - .agpr_count:     0
    .args:
      - .actual_access:  read_only
        .address_space:  global
        .offset:         0
        .size:           8
        .value_kind:     global_buffer
      - .actual_access:  read_only
        .address_space:  global
        .offset:         8
        .size:           8
        .value_kind:     global_buffer
      - .actual_access:  write_only
        .address_space:  global
        .offset:         16
        .size:           8
        .value_kind:     global_buffer
      - .actual_access:  write_only
        .address_space:  global
        .offset:         24
        .size:           8
        .value_kind:     global_buffer
      - .actual_access:  write_only
        .address_space:  global
        .offset:         32
        .size:           8
        .value_kind:     global_buffer
    .group_segment_fixed_size: 1024
    .kernarg_segment_align: 8
    .kernarg_segment_size: 40
    .language:       OpenCL C
    .language_version:
      - 2
      - 0
    .max_flat_workgroup_size: 256
    .name:           _Z7k1_packPKfS0_PmPiP15HIP_vector_typeIfLj4EE
    .private_segment_fixed_size: 0
    .sgpr_count:     16
    .sgpr_spill_count: 0
    .symbol:         _Z7k1_packPKfS0_PmPiP15HIP_vector_typeIfLj4EE.kd
    .uniform_work_group_size: 1
    .uses_dynamic_stack: false
    .vgpr_count:     33
    .vgpr_spill_count: 0
    .wavefront_size: 64
  - .agpr_count:     0
    .args:
      - .actual_access:  read_only
        .address_space:  global
        .offset:         0
        .size:           8
        .value_kind:     global_buffer
      - .actual_access:  read_only
        .address_space:  global
        .offset:         8
        .size:           8
        .value_kind:     global_buffer
      - .actual_access:  write_only
        .address_space:  global
        .offset:         16
        .size:           8
        .value_kind:     global_buffer
      - .actual_access:  read_only
        .address_space:  global
        .offset:         24
        .size:           8
        .value_kind:     global_buffer
      - .actual_access:  write_only
        .address_space:  global
        .offset:         32
        .size:           8
        .value_kind:     global_buffer
      - .actual_access:  write_only
        .address_space:  global
        .offset:         40
        .size:           8
        .value_kind:     global_buffer
      - .actual_access:  read_only
        .address_space:  global
        .offset:         48
        .size:           8
        .value_kind:     global_buffer
      - .address_space:  global
        .offset:         56
        .size:           8
        .value_kind:     global_buffer
      - .actual_access:  write_only
        .address_space:  global
        .offset:         64
        .size:           8
        .value_kind:     global_buffer
      - .actual_access:  write_only
        .address_space:  global
        .offset:         72
        .size:           8
        .value_kind:     global_buffer
    .group_segment_fixed_size: 34880
    .kernarg_segment_align: 8
    .kernarg_segment_size: 80
    .language:       OpenCL C
    .language_version:
      - 2
      - 0
    .max_flat_workgroup_size: 512
    .name:           _Z7k2_elimPKjPKiPiS2_PfP15HIP_vector_typeIiLj4EEPKfS4_PtSA_
    .private_segment_fixed_size: 0
    .sgpr_count:     50
    .sgpr_spill_count: 0
    .symbol:         _Z7k2_elimPKjPKiPiS2_PfP15HIP_vector_typeIiLj4EEPKfS4_PtSA_.kd
    .uniform_work_group_size: 1
    .uses_dynamic_stack: false
    .vgpr_count:     35
    .vgpr_spill_count: 0
    .wavefront_size: 64
  - .agpr_count:     0
    .args:
      - .actual_access:  read_only
        .address_space:  global
        .offset:         0
        .size:           8
        .value_kind:     global_buffer
      - .actual_access:  read_only
        .address_space:  global
        .offset:         8
        .size:           8
        .value_kind:     global_buffer
      - .actual_access:  read_only
        .address_space:  global
        .offset:         16
        .size:           8
        .value_kind:     global_buffer
      - .actual_access:  read_only
        .address_space:  global
        .offset:         24
        .size:           8
        .value_kind:     global_buffer
      - .actual_access:  read_only
        .address_space:  global
        .offset:         32
        .size:           8
        .value_kind:     global_buffer
      - .actual_access:  read_only
        .address_space:  global
        .offset:         40
        .size:           8
        .value_kind:     global_buffer
      - .actual_access:  write_only
        .address_space:  global
        .offset:         48
        .size:           8
        .value_kind:     global_buffer
    .group_segment_fixed_size: 80064
    .kernarg_segment_align: 8
    .kernarg_segment_size: 56
    .language:       OpenCL C
    .language_version:
      - 2
      - 0
    .max_flat_workgroup_size: 256
    .name:           _Z8k3_chainPKfPK15HIP_vector_typeIiLj4EEPKtS6_S0_S0_Pf
    .private_segment_fixed_size: 0
    .sgpr_count:     28
    .sgpr_spill_count: 0
    .symbol:         _Z8k3_chainPKfPK15HIP_vector_typeIiLj4EEPKtS6_S0_S0_Pf.kd
    .uniform_work_group_size: 1
    .uses_dynamic_stack: false
    .vgpr_count:     184
    .vgpr_spill_count: 0
    .wavefront_size: 64
